# k_fine: exact touch-prefetch of each chunk's csorted run right after its loff entry arrives (4 barriers before the staging loads)
# speedup vs baseline: 1.0014x; 1.0014x over previous
_Z6k_finePKjPKtPiPt:
	s_movk_i32 s3, 0x100
	v_cmp_gt_u32_e32 vcc, s3, v0
	v_mov_b32_e32 v26, 0
	v_mov_b32_e32 v8, 0
	s_and_saveexec_b64 s[4:5], vcc
	s_cbranch_execz .LBB0_2
	s_load_dwordx2 s[6:7], s[0:1], 0x8
	s_load_dwordx2 s[60:61], s[0:1], 0x0
	s_movk_i32 s3, 0x188
	v_mov_b32_e32 v1, s2
	v_mad_u32_u24 v2, v0, s3, v1
	v_ashrrev_i32_e32 v3, 31, v2
	s_waitcnt lgkmcnt(0)
	v_lshl_add_u64 v[2:3], v[2:3], 1, s[6:7]
	global_load_dword v1, v[2:3], off
	s_waitcnt vmcnt(0)
	v_and_b32_e32 v8, 0xffff, v1
	v_sub_u32_sdwa v26, v1, v8 dst_sel:DWORD dst_unused:UNUSED_PAD src0_sel:WORD_1 src1_sel:DWORD
	v_mul_u32_u24_e32 v2, 0x186c, v0
	v_add_u32_e32 v2, v2, v8
	v_lshlrev_b32_e32 v2, 2, v2
	v_lshl_add_u32 v3, v26, 2, v2
	v_add_u32_e32 v3, -4, v3
	v_max_i32_e32 v3, v3, v2
	global_load_dword v55, v2, s[60:61]
	global_load_dword v55, v3, s[60:61]

	.amdhsa_kernel _Z6k_finePKjPKtPiPt
		.amdhsa_group_segment_fixed_size 32320
		.amdhsa_private_segment_fixed_size 0
		.amdhsa_kernarg_size 32
		.amdhsa_user_sgpr_count 2
		.amdhsa_user_sgpr_dispatch_ptr 0
		.amdhsa_user_sgpr_queue_ptr 0
		.amdhsa_user_sgpr_kernarg_segment_ptr 1
		.amdhsa_user_sgpr_dispatch_id 0
		.amdhsa_user_sgpr_kernarg_preload_length 0
		.amdhsa_user_sgpr_kernarg_preload_offset 0
		.amdhsa_user_sgpr_private_segment_size 0
		.amdhsa_uses_dynamic_stack 0
		.amdhsa_enable_private_segment 0
		.amdhsa_system_sgpr_workgroup_id_x 1
		.amdhsa_system_sgpr_workgroup_id_y 0
		.amdhsa_system_sgpr_workgroup_id_z 0
		.amdhsa_system_sgpr_workgroup_info 0
		.amdhsa_system_vgpr_workitem_id 0
		.amdhsa_next_free_vgpr 56
		.amdhsa_next_free_sgpr 65
		.amdhsa_accum_offset 56
		.amdhsa_reserve_vcc 1
		.amdhsa_float_round_mode_32 0
		.amdhsa_float_round_mode_16_64 0
		.amdhsa_float_denorm_mode_32 3
		.amdhsa_float_denorm_mode_16_64 3
		.amdhsa_dx10_clamp 1
		.amdhsa_ieee_mode 1
		.amdhsa_fp16_overflow 0
		.amdhsa_tg_split 0
		.amdhsa_exception_fp_ieee_invalid_op 0
		.amdhsa_exception_fp_denorm_src 0
		.amdhsa_exception_fp_ieee_div_zero 0
		.amdhsa_exception_fp_ieee_overflow 0
		.amdhsa_exception_fp_ieee_underflow 0
		.amdhsa_exception_fp_ieee_inexact 0
		.amdhsa_exception_int_div_zero 0
	.end_amdhsa_kernel

amdhsa.kernels:
  - .agpr_count:     0
    .args:
      - .actual_access:  read_only
        .address_space:  global
        .offset:         0
        .size:           8
        .value_kind:     global_buffer
      - .actual_access:  read_only
        .address_space:  global
        .offset:         8
        .size:           8
        .value_kind:     global_buffer
      - .actual_access:  write_only
        .address_space:  global
        .offset:         16
        .size:           8
        .value_kind:     global_buffer
      - .actual_access:  write_only
        .address_space:  global
        .offset:         24
        .size:           8
        .value_kind:     global_buffer
    .group_segment_fixed_size: 32320
    .kernarg_segment_align: 8
    .kernarg_segment_size: 32
    .language:       OpenCL C
    .language_version:
      - 2
      - 0
    .max_flat_workgroup_size: 1024
    .name:           _Z6k_finePKjPKtPiPt
    .private_segment_fixed_size: 0
    .sgpr_count:     71
    .sgpr_spill_count: 0
    .symbol:         _Z6k_finePKjPKtPiPt.kd
    .uniform_work_group_size: 1
    .uses_dynamic_stack: false
    .vgpr_count:     56
    .vgpr_spill_count: 0
    .wavefront_size: 64
  - .agpr_count:     0
    .args:
      - .actual_access:  read_only
        .address_space:  global
        .offset:         0
        .size:           8
        .value_kind:     global_buffer
      - .actual_access:  read_only
        .address_space:  global
        .offset:         8
        .size:           8
        .value_kind:     global_buffer
      - .actual_access:  write_only
        .address_space:  global
        .offset:         16
        .size:           8
        .value_kind:     global_buffer
      - .actual_access:  write_only
        .address_space:  global
        .offset:         24
        .size:           8
        .value_kind:     global_buffer
      - .actual_access:  read_only
        .address_space:  global
        .offset:         32
        .size:           8
        .value_kind:     global_buffer
      - .actual_access:  read_only
        .address_space:  global
        .offset:         40
        .size:           8
        .value_kind:     global_buffer
      - .actual_access:  write_only
        .address_space:  global
        .offset:         48
        .size:           8
        .value_kind:     global_buffer
      - .actual_access:  write_only
        .address_space:  global
        .offset:         56
        .size:           8
        .value_kind:     global_buffer
      - .actual_access:  read_only
        .address_space:  global
        .offset:         64
        .size:           8
        .value_kind:     global_buffer
      - .actual_access:  read_only
        .address_space:  global
        .offset:         72
        .size:           8
        .value_kind:     global_buffer
      - .actual_access:  read_only
        .address_space:  global
        .offset:         80
        .size:           8
        .value_kind:     global_buffer
      - .actual_access:  write_only
        .address_space:  global
        .offset:         88
        .size:           8
        .value_kind:     global_buffer
      - .actual_access:  write_only
        .address_space:  global
        .offset:         96
        .size:           8
        .value_kind:     global_buffer
      - .actual_access:  write_only
        .address_space:  global
        .offset:         104
        .size:           8
        .value_kind:     global_buffer
    .group_segment_fixed_size: 53248
    .kernarg_segment_align: 8
    .kernarg_segment_size: 112
    .language:       OpenCL C
    .language_version:
      - 2
      - 0
    .max_flat_workgroup_size: 256
    .name:           _Z8k_stageAPKiS0_PjPtPKfS4_PDF16_S5_S4_S4_S4_S5_PfS6_
    .private_segment_fixed_size: 0
    .sgpr_count:     75
    .sgpr_spill_count: 0
    .symbol:         _Z8k_stageAPKiS0_PjPtPKfS4_PDF16_S5_S4_S4_S4_S5_PfS6_.kd
    .uniform_work_group_size: 1
    .uses_dynamic_stack: false
    .vgpr_count:     158
    .vgpr_spill_count: 0
    .wavefront_size: 64
  - .agpr_count:     4
    .args:
      - .actual_access:  read_only
        .address_space:  global
        .offset:         0
        .size:           8
        .value_kind:     global_buffer
      - .actual_access:  read_only
        .address_space:  global
        .offset:         8
        .size:           8
        .value_kind:     global_buffer
      - .actual_access:  read_only
        .address_space:  global
        .offset:         16
        .size:           8
        .value_kind:     global_buffer
      - .actual_access:  read_only
        .address_space:  global
        .offset:         24
        .size:           8
        .value_kind:     global_buffer
      - .actual_access:  write_only
        .address_space:  global
        .offset:         32
        .size:           8
        .value_kind:     global_buffer
      - .actual_access:  write_only
        .address_space:  global
        .offset:         40
        .size:           8
        .value_kind:     global_buffer
      - .actual_access:  write_only
        .address_space:  global
        .offset:         48
        .size:           8
        .value_kind:     global_buffer
    .group_segment_fixed_size: 19584
    .kernarg_segment_align: 8
    .kernarg_segment_size: 56
    .language:       OpenCL C
    .language_version:
      - 2
      - 0
    .max_flat_workgroup_size: 256
    .name:           _Z7k_gemm2PKDF16_S0_PKfS2_PDF16_PfS4_
    .private_segment_fixed_size: 0
    .sgpr_count:     30
    .sgpr_spill_count: 0
    .symbol:         _Z7k_gemm2PKDF16_S0_PKfS2_PDF16_PfS4_.kd
    .uniform_work_group_size: 1
    .uses_dynamic_stack: false
    .vgpr_count:     84
    .vgpr_spill_count: 0
    .wavefront_size: 64
  - .agpr_count:     12
    .args:
      - .actual_access:  read_only
        .address_space:  global
        .offset:         0
        .size:           8
        .value_kind:     global_buffer
      - .actual_access:  read_only
        .address_space:  global
        .offset:         8
        .size:           8
        .value_kind:     global_buffer
      - .actual_access:  read_only
        .address_space:  global
        .offset:         16
        .size:           8
        .value_kind:     global_buffer
      - .actual_access:  read_only
        .address_space:  global
        .offset:         24
        .size:           8
        .value_kind:     global_buffer
      - .actual_access:  read_only
        .address_space:  global
        .offset:         32
        .size:           8
        .value_kind:     global_buffer
      - .actual_access:  read_only
        .address_space:  global
        .offset:         40
        .size:           8
        .value_kind:     global_buffer
      - .actual_access:  read_only
        .address_space:  global
        .offset:         48
        .size:           8
        .value_kind:     global_buffer
      - .actual_access:  read_only
        .address_space:  global
        .offset:         56
        .size:           8
        .value_kind:     global_buffer
      - .actual_access:  read_only
        .address_space:  global
        .offset:         64
        .size:           8
        .value_kind:     global_buffer
      - .actual_access:  read_only
        .address_space:  global
        .offset:         72
        .size:           8
        .value_kind:     global_buffer
      - .actual_access:  write_only
        .address_space:  global
        .offset:         80
        .size:           8
        .value_kind:     global_buffer
      - .actual_access:  write_only
        .address_space:  global
        .offset:         88
        .size:           8
        .value_kind:     global_buffer
      - .actual_access:  write_only
        .address_space:  global
        .offset:         96
        .size:           8
        .value_kind:     global_buffer
      - .offset:         104
        .size:           4
        .value_kind:     hidden_block_count_x
      - .offset:         108
        .size:           4
        .value_kind:     hidden_block_count_y
      - .offset:         112
        .size:           4
        .value_kind:     hidden_block_count_z
      - .offset:         116
        .size:           2
        .value_kind:     hidden_group_size_x
      - .offset:         118
        .size:           2
        .value_kind:     hidden_group_size_y
      - .offset:         120
        .size:           2
        .value_kind:     hidden_group_size_z
      - .offset:         122
        .size:           2
        .value_kind:     hidden_remainder_x
      - .offset:         124
        .size:           2
        .value_kind:     hidden_remainder_y
      - .offset:         126
        .size:           2
        .value_kind:     hidden_remainder_z
      - .offset:         144
        .size:           8
        .value_kind:     hidden_global_offset_x
      - .offset:         152
        .size:           8
        .value_kind:     hidden_global_offset_y
      - .offset:         160
        .size:           8
        .value_kind:     hidden_global_offset_z
      - .offset:         168
        .size:           2
        .value_kind:     hidden_grid_dims
    .group_segment_fixed_size: 39168
    .kernarg_segment_align: 8
    .kernarg_segment_size: 360
    .language:       OpenCL C
    .language_version:
      - 2
      - 0
    .max_flat_workgroup_size: 256
    .name:           _Z5k_aggILi4ELi128ELi16ELi16ELb0EEvPKiPKtPKDF16_PKfS7_S7_PvS5_S7_S7_PDF16_PfSA_
    .private_segment_fixed_size: 0
    .sgpr_count:     55
    .sgpr_spill_count: 0
    .symbol:         _Z5k_aggILi4ELi128ELi16ELi16ELb0EEvPKiPKtPKDF16_PKfS7_S7_PvS5_S7_S7_PDF16_PfSA_.kd
    .uniform_work_group_size: 1
    .uses_dynamic_stack: false
    .vgpr_count:     124
    .vgpr_spill_count: 0
    .wavefront_size: 64
  - .agpr_count:     0
    .args:
      - .actual_access:  read_only
        .address_space:  global
        .offset:         0
        .size:           8
        .value_kind:     global_buffer
      - .actual_access:  read_only
        .address_space:  global
        .offset:         8
        .size:           8
        .value_kind:     global_buffer
      - .actual_access:  read_only
        .address_space:  global
        .offset:         16
        .size:           8
        .value_kind:     global_buffer
      - .actual_access:  read_only
        .address_space:  global
        .offset:         24
        .size:           8
        .value_kind:     global_buffer
      - .actual_access:  read_only
        .address_space:  global
        .offset:         32
        .size:           8
        .value_kind:     global_buffer
      - .actual_access:  read_only
        .address_space:  global
        .offset:         40
        .size:           8
        .value_kind:     global_buffer
      - .actual_access:  write_only
        .address_space:  global
        .offset:         48
        .size:           8
        .value_kind:     global_buffer
      - .actual_access:  read_only
        .address_space:  global
        .offset:         56
        .size:           8
        .value_kind:     global_buffer
      - .actual_access:  read_only
        .address_space:  global
        .offset:         64
        .size:           8
        .value_kind:     global_buffer
      - .actual_access:  read_only
        .address_space:  global
        .offset:         72
        .size:           8
        .value_kind:     global_buffer
      - .actual_access:  read_only
        .address_space:  global
        .offset:         80
        .size:           8
        .value_kind:     global_buffer
      - .actual_access:  read_only
        .address_space:  global
        .offset:         88
        .size:           8
        .value_kind:     global_buffer
      - .actual_access:  read_only
        .address_space:  global
        .offset:         96
        .size:           8
        .value_kind:     global_buffer
      - .offset:         104
        .size:           4
        .value_kind:     hidden_block_count_x
      - .offset:         108
        .size:           4
        .value_kind:     hidden_block_count_y
      - .offset:         112
        .size:           4
        .value_kind:     hidden_block_count_z
      - .offset:         116
        .size:           2
        .value_kind:     hidden_group_size_x
      - .offset:         118
        .size:           2
        .value_kind:     hidden_group_size_y
      - .offset:         120
        .size:           2
        .value_kind:     hidden_group_size_z
      - .offset:         122
        .size:           2
        .value_kind:     hidden_remainder_x
      - .offset:         124
        .size:           2
        .value_kind:     hidden_remainder_y
      - .offset:         126
        .size:           2
        .value_kind:     hidden_remainder_z
      - .offset:         144
        .size:           8
        .value_kind:     hidden_global_offset_x
      - .offset:         152
        .size:           8
        .value_kind:     hidden_global_offset_y
      - .offset:         160
        .size:           8
        .value_kind:     hidden_global_offset_z
      - .offset:         168
        .size:           2
        .value_kind:     hidden_grid_dims
    .group_segment_fixed_size: 8704
    .kernarg_segment_align: 8
    .kernarg_segment_size: 360
    .language:       OpenCL C
    .language_version:
      - 2
      - 0
    .max_flat_workgroup_size: 256
    .name:           _Z5k_aggILi1ELi40ELi5ELi5ELb1EEvPKiPKtPKDF16_PKfS7_S7_PvS5_S7_S7_PDF16_PfSA_
    .private_segment_fixed_size: 0
    .sgpr_count:     46
    .sgpr_spill_count: 0
    .symbol:         _Z5k_aggILi1ELi40ELi5ELi5ELb1EEvPKiPKtPKDF16_PKfS7_S7_PvS5_S7_S7_PDF16_PfSA_.kd
    .uniform_work_group_size: 1
    .uses_dynamic_stack: false
    .vgpr_count:     80
    .vgpr_spill_count: 0
    .wavefront_size: 64
